# scan state: y sum and its LDS store moved ahead of the decay multiplies (YB product issued before the H updates) so the store latency hides under them; on top of scalar adds, static GEMM priority, GEM
# baseline (speedup 1.0000x reference)
.LBB0_1114:
	v_writelane_b32 v255, s0, 11
	s_and_b32 s5, s0, 1
	v_readlane_b32 s0, v254, 35
	v_readlane_b32 s1, v254, 36
	s_andn2_b64 vcc, exec, s[0:1]
	s_mov_b64 s[76:77], -1
	v_cndmask_b32_e64 v194, 0, 1, s[0:1]
	v_cmp_ne_u32_e64 s[8:9], 1, v194
	s_mul_i32 s0, s5, 0x1e00
	v_writelane_b32 v255, s8, 17
	v_writelane_b32 v255, s9, 18
	v_writelane_b32 v255, s5, 13
	s_cbranch_vccnz .LBB0_1116
	v_readlane_b32 s0, v255, 13
	s_nop 1
	s_nop 0
	s_mul_i32 s1, s0, 0x1e00
	s_lshl_b32 s0, s0, 13
	v_add_u32_e32 v252, s1, v166
	v_add_u32_e32 v253, s0, v165
	ds_read2_b64 v[68:71], v252 offset1:80
	v_cvt_pk_bf16_f32 v198, v2, v3
	v_cvt_pk_bf16_f32 v199, v4, v5
	v_cvt_pk_bf16_f32 v202, v10, v11
	v_cvt_pk_bf16_f32 v203, v12, v13
	v_cvt_pk_bf16_f32 v200, v6, v7
	v_cvt_pk_bf16_f32 v201, v8, v9
	v_cvt_pk_bf16_f32 v204, v14, v15
	v_cvt_pk_bf16_f32 v205, v16, v17
	ds_read2_b64 v[26:29], v247 offset1:4
	ds_read2_b64 v[30:33], v247 offset0:8 offset1:12
	ds_read2_b64 v[72:75], v252 offset0:160 offset1:240
	v_mfma_f32_16x16x16_bf16 v[206:209], v[18:19], v[198:199], 0
	v_mfma_f32_16x16x16_bf16 v[210:213], v[22:23], v[202:203], 0
	ds_read_b64_tr_b16 v[34:35], v248 offset:9216
	ds_read_b64_tr_b16 v[36:37], v248 offset:9248
	ds_read_b64_tr_b16 v[38:39], v248 offset:9280
	ds_read_b64_tr_b16 v[40:41], v248 offset:9312
	v_mfma_f32_16x16x16_bf16 v[206:209], v[20:21], v[200:201], v[206:209]
	v_mfma_f32_16x16x16_bf16 v[210:213], v[24:25], v[204:205], v[210:213]
	ds_read_b64_tr_b16 v[42:43], v248 offset:13824
	ds_read_b64_tr_b16 v[44:45], v248 offset:13856
	ds_read_b64_tr_b16 v[46:47], v248 offset:13888
	ds_read_b64_tr_b16 v[48:49], v248 offset:13920
	s_waitcnt lgkmcnt(11)
	v_mfma_f32_16x16x16_bf16 v[210:213], v[68:69], v[66:67], v[210:213]
	s_waitcnt lgkmcnt(10)
	v_mfma_f32_16x16x16_bf16 v[214:217], v[26:27], v[198:199], 0
	s_waitcnt lgkmcnt(9)
	v_mfma_f32_16x16x16_bf16 v[218:221], v[30:31], v[202:203], 0
	v_mfma_f32_16x16x16_bf16 v[214:217], v[28:29], v[200:201], v[214:217]
	v_mfma_f32_16x16x16_bf16 v[218:221], v[32:33], v[204:205], v[218:221]
	ds_read_b32 v50, v251 offset:33792
	ds_read_b32 v51, v251 offset:34048
	v_add_u32_e32 v246, 0x900, v246
	ds_read2_b64 v[76:79], v246 offset1:4
	ds_read2_b64 v[80:83], v246 offset0:8 offset1:12
	v_add_f32_e32 v206, v206, v210
	v_add_f32_e32 v207, v207, v211
	v_add_f32_e32 v208, v208, v212
	v_add_f32_e32 v209, v209, v213
	v_cvt_pk_bf16_f32 v242, v206, v207
	v_cvt_pk_bf16_f32 v243, v208, v209
	ds_read_b64_tr_b16 v[84:85], v250 offset:20736
	v_add_u32_e32 v252, 0xf00, v252
	s_waitcnt lgkmcnt(13)
	ds_read2_b64 v[86:89], v252 offset1:80
	v_mfma_f32_16x16x16_bf16 v[238:241], v[74:75], v[242:243], 0
	v_mfma_f32_16x16x16_bf16 v[214:217], v[70:71], v[66:67], v[214:217]
	s_waitcnt lgkmcnt(12)
	v_mfma_f32_16x16x16_bf16 v[2:5], v[34:35], v[66:67], v[2:5]
	v_mfma_f32_16x16x16_bf16 v[6:9], v[36:37], v[66:67], v[6:9]
	s_waitcnt lgkmcnt(10)
	v_mfma_f32_16x16x16_bf16 v[10:13], v[38:39], v[66:67], v[10:13]
	v_mfma_f32_16x16x16_bf16 v[14:17], v[40:41], v[66:67], v[14:17]
	ds_read2_b64 v[90:93], v252 offset0:160 offset1:240
	v_add_u32_e32 v247, 0x900, v247
	ds_read2_b64 v[26:29], v247 offset1:4
	ds_read2_b64 v[30:33], v247 offset0:8 offset1:12
	v_cvt_pk_bf16_f32 v244, -v238, -v239
	v_cvt_pk_bf16_f32 v245, -v240, -v241
	ds_read_b64_tr_b16 v[34:35], v248 offset:11520
	s_waitcnt lgkmcnt(13)
	ds_read_b64_tr_b16 v[36:37], v248 offset:11552
	s_waitcnt lgkmcnt(13)
	ds_read_b64_tr_b16 v[38:39], v248 offset:11584
	s_waitcnt lgkmcnt(13)
	ds_read_b64_tr_b16 v[40:41], v248 offset:11616
	v_mfma_f32_16x16x16_bf16 v[218:221], v[72:73], v[244:245], v[218:221]
	v_mfma_f32_16x16x16_bf16 v[2:5], v[42:43], v[244:245], v[2:5]
	v_mfma_f32_16x16x16_bf16 v[6:9], v[44:45], v[244:245], v[6:9]
	s_waitcnt lgkmcnt(13)
	v_mfma_f32_16x16x16_bf16 v[10:13], v[46:47], v[244:245], v[10:13]
	v_mfma_f32_16x16x16_bf16 v[14:17], v[48:49], v[244:245], v[14:17]
	ds_read_b64_tr_b16 v[42:43], v248 offset:16128
	s_waitcnt lgkmcnt(13)
	ds_read_b64_tr_b16 v[44:45], v248 offset:16160
	s_waitcnt lgkmcnt(13)
	ds_read_b64_tr_b16 v[46:47], v248 offset:16192
	s_waitcnt lgkmcnt(13)
	ds_read_b64_tr_b16 v[48:49], v248 offset:16224
	v_add_f32_e32 v214, v214, v218
	v_add_f32_e32 v215, v215, v219
	v_add_f32_e32 v216, v216, v220
	v_add_f32_e32 v217, v217, v221
	s_waitcnt lgkmcnt(13)
	ds_write2st64_b32 v253, v214, v215 offset0:0 offset1:1
	s_waitcnt lgkmcnt(13)
	ds_write2st64_b32 v253, v216, v217 offset0:2 offset1:3
	v_mul_f32_dpp v2, v50, v2 row_newbcast:0 row_mask:0xf bank_mask:0xf
	v_mul_f32_dpp v3, v50, v3 row_newbcast:1 row_mask:0xf bank_mask:0xf
	v_mul_f32_dpp v4, v50, v4 row_newbcast:2 row_mask:0xf bank_mask:0xf
	v_mul_f32_dpp v5, v50, v5 row_newbcast:3 row_mask:0xf bank_mask:0xf
	v_mul_f32_dpp v6, v50, v6 row_newbcast:4 row_mask:0xf bank_mask:0xf
	v_mul_f32_dpp v7, v50, v7 row_newbcast:5 row_mask:0xf bank_mask:0xf
	v_mul_f32_dpp v8, v50, v8 row_newbcast:6 row_mask:0xf bank_mask:0xf
	v_mul_f32_dpp v9, v50, v9 row_newbcast:7 row_mask:0xf bank_mask:0xf
	v_mul_f32_dpp v10, v50, v10 row_newbcast:8 row_mask:0xf bank_mask:0xf
	v_mul_f32_dpp v11, v50, v11 row_newbcast:9 row_mask:0xf bank_mask:0xf
	v_mul_f32_dpp v12, v50, v12 row_newbcast:10 row_mask:0xf bank_mask:0xf
	v_mul_f32_dpp v13, v50, v13 row_newbcast:11 row_mask:0xf bank_mask:0xf
	v_mul_f32_dpp v14, v50, v14 row_newbcast:12 row_mask:0xf bank_mask:0xf
	v_mul_f32_dpp v15, v50, v15 row_newbcast:13 row_mask:0xf bank_mask:0xf
	v_mul_f32_dpp v16, v50, v16 row_newbcast:14 row_mask:0xf bank_mask:0xf
	v_mul_f32_dpp v17, v50, v17 row_newbcast:15 row_mask:0xf bank_mask:0xf
	v_cvt_pk_bf16_f32 v198, v2, v3
	v_cvt_pk_bf16_f32 v199, v4, v5
	v_cvt_pk_bf16_f32 v202, v10, v11
	v_cvt_pk_bf16_f32 v203, v12, v13
	v_cvt_pk_bf16_f32 v200, v6, v7
	v_cvt_pk_bf16_f32 v201, v8, v9
	v_cvt_pk_bf16_f32 v204, v14, v15
	v_cvt_pk_bf16_f32 v205, v16, v17
	v_add_u32_e32 v246, v115, v155
	v_bfe_u32 v248, v0, 4, 2
	v_mul_u32_u24_e32 v248, 0x240, v248
	v_bfe_u32 v249, v0, 2, 2
	v_mul_u32_u24_e32 v249, 0x90, v249
	v_and_b32_e32 v250, 3, v0
	v_add_u32_e32 v248, v248, v249
	v_lshl_add_u32 v248, v250, 3, v248
	v_bfe_u32 v249, v0, 6, 2
	v_add_u32_e32 v246, 0x8600, v246
	v_add_u32_e32 v248, 0x8600, v248
	v_and_b32_e32 v251, 12, v0
	v_lshl_add_u32 v251, v251, 4, v113
	v_lshl_add_u32 v251, v250, 2, v251
	v_add_u32_e32 v251, 0x8600, v251
	v_lshl_add_u32 v250, v249, 5, v248
	v_add_u32_e32 v247, 0x1200, v246
	s_waitcnt lgkmcnt(13)
	ds_read2_b64 v[18:21], v246 offset1:4
	s_waitcnt lgkmcnt(13)
	ds_read2_b64 v[22:25], v246 offset0:8 offset1:12
	s_waitcnt lgkmcnt(13)
	ds_read_b64_tr_b16 v[66:67], v250 offset:18432
	v_mfma_f32_16x16x16_bf16 v[206:209], v[76:77], v[198:199], 0
	v_mfma_f32_16x16x16_bf16 v[210:213], v[80:81], v[202:203], 0
	v_mfma_f32_16x16x16_bf16 v[206:209], v[78:79], v[200:201], v[206:209]
	v_mfma_f32_16x16x16_bf16 v[210:213], v[82:83], v[204:205], v[210:213]
	v_mfma_f32_16x16x16_bf16 v[210:213], v[86:87], v[84:85], v[210:213]
	v_mfma_f32_16x16x16_bf16 v[214:217], v[26:27], v[198:199], 0
	s_waitcnt lgkmcnt(13)
	v_mfma_f32_16x16x16_bf16 v[218:221], v[30:31], v[202:203], 0
	v_mfma_f32_16x16x16_bf16 v[214:217], v[28:29], v[200:201], v[214:217]
	v_mfma_f32_16x16x16_bf16 v[218:221], v[32:33], v[204:205], v[218:221]
	s_nop 2
	v_add_f32_e32 v206, v206, v210
	v_add_f32_e32 v207, v207, v211
	v_add_f32_e32 v208, v208, v212
	v_add_f32_e32 v209, v209, v213
	v_cvt_pk_bf16_f32 v242, v206, v207
	v_cvt_pk_bf16_f32 v243, v208, v209
	s_nop 1
	v_mfma_f32_16x16x16_bf16 v[238:241], v[92:93], v[242:243], 0
	v_mfma_f32_16x16x16_bf16 v[214:217], v[88:89], v[84:85], v[214:217]
	s_waitcnt lgkmcnt(11)
	v_mfma_f32_16x16x16_bf16 v[2:5], v[34:35], v[84:85], v[2:5]
	v_mfma_f32_16x16x16_bf16 v[6:9], v[36:37], v[84:85], v[6:9]
	s_waitcnt lgkmcnt(9)
	v_mfma_f32_16x16x16_bf16 v[10:13], v[38:39], v[84:85], v[10:13]
	v_mfma_f32_16x16x16_bf16 v[14:17], v[40:41], v[84:85], v[14:17]
	s_nop 0
	v_cvt_pk_bf16_f32 v244, -v238, -v239
	v_cvt_pk_bf16_f32 v245, -v240, -v241
	s_nop 1
	v_mfma_f32_16x16x16_bf16 v[218:221], v[90:91], v[244:245], v[218:221]
	s_waitcnt lgkmcnt(7)
	v_mfma_f32_16x16x16_bf16 v[2:5], v[42:43], v[244:245], v[2:5]
	v_mfma_f32_16x16x16_bf16 v[6:9], v[44:45], v[244:245], v[6:9]
	s_waitcnt lgkmcnt(5)
	v_mfma_f32_16x16x16_bf16 v[10:13], v[46:47], v[244:245], v[10:13]
	v_mfma_f32_16x16x16_bf16 v[14:17], v[48:49], v[244:245], v[14:17]
	s_nop 1
	v_add_f32_e32 v214, v214, v218
	v_add_f32_e32 v215, v215, v219
	v_add_f32_e32 v216, v216, v220
	v_add_f32_e32 v217, v217, v221
	ds_write2st64_b32 v253, v214, v215 offset0:16 offset1:17
	ds_write2st64_b32 v253, v216, v217 offset0:18 offset1:19
	v_mul_f32_dpp v2, v51, v2 row_newbcast:0 row_mask:0xf bank_mask:0xf
	v_mul_f32_dpp v3, v51, v3 row_newbcast:1 row_mask:0xf bank_mask:0xf
	v_mul_f32_dpp v4, v51, v4 row_newbcast:2 row_mask:0xf bank_mask:0xf
	v_mul_f32_dpp v5, v51, v5 row_newbcast:3 row_mask:0xf bank_mask:0xf
	v_mul_f32_dpp v6, v51, v6 row_newbcast:4 row_mask:0xf bank_mask:0xf
	v_mul_f32_dpp v7, v51, v7 row_newbcast:5 row_mask:0xf bank_mask:0xf
	v_mul_f32_dpp v8, v51, v8 row_newbcast:6 row_mask:0xf bank_mask:0xf
	v_mul_f32_dpp v9, v51, v9 row_newbcast:7 row_mask:0xf bank_mask:0xf
	v_mul_f32_dpp v10, v51, v10 row_newbcast:8 row_mask:0xf bank_mask:0xf
	v_mul_f32_dpp v11, v51, v11 row_newbcast:9 row_mask:0xf bank_mask:0xf
	v_mul_f32_dpp v12, v51, v12 row_newbcast:10 row_mask:0xf bank_mask:0xf
	v_mul_f32_dpp v13, v51, v13 row_newbcast:11 row_mask:0xf bank_mask:0xf
	v_mul_f32_dpp v14, v51, v14 row_newbcast:12 row_mask:0xf bank_mask:0xf
	v_mul_f32_dpp v15, v51, v15 row_newbcast:13 row_mask:0xf bank_mask:0xf
	v_mul_f32_dpp v16, v51, v16 row_newbcast:14 row_mask:0xf bank_mask:0xf
	v_mul_f32_dpp v17, v51, v17 row_newbcast:15 row_mask:0xf bank_mask:0xf
	s_branch .Lscan_join1

.LBB0_1140:
.Lscan_join1:
	s_waitcnt lgkmcnt(0)
	s_barrier
	v_readlane_b32 s0, v255, 17
	v_readlane_b32 s1, v255, 18
	s_and_b64 vcc, exec, s[0:1]
	s_mov_b64 s[76:77], -1
	s_cbranch_vccnz .LBB0_1142
	v_readlane_b32 s0, v255, 13
	s_nop 1
	s_xor_b32 s0, s0, 1
	s_mul_i32 s1, s0, 0x1e00
	s_lshl_b32 s0, s0, 13
	v_add_u32_e32 v252, s1, v166
	v_add_u32_e32 v253, s0, v165
	ds_read2_b64 v[68:71], v252 offset1:80
	v_cvt_pk_bf16_f32 v198, v2, v3
	v_cvt_pk_bf16_f32 v199, v4, v5
	v_cvt_pk_bf16_f32 v202, v10, v11
	v_cvt_pk_bf16_f32 v203, v12, v13
	v_cvt_pk_bf16_f32 v200, v6, v7
	v_cvt_pk_bf16_f32 v201, v8, v9
	v_cvt_pk_bf16_f32 v204, v14, v15
	v_cvt_pk_bf16_f32 v205, v16, v17
	ds_read2_b64 v[26:29], v247 offset1:4
	ds_read2_b64 v[30:33], v247 offset0:8 offset1:12
	ds_read2_b64 v[72:75], v252 offset0:160 offset1:240
	v_mfma_f32_16x16x16_bf16 v[206:209], v[18:19], v[198:199], 0
	v_mfma_f32_16x16x16_bf16 v[210:213], v[22:23], v[202:203], 0
	ds_read_b64_tr_b16 v[34:35], v248 offset:9216
	ds_read_b64_tr_b16 v[36:37], v248 offset:9248
	ds_read_b64_tr_b16 v[38:39], v248 offset:9280
	ds_read_b64_tr_b16 v[40:41], v248 offset:9312
	v_mfma_f32_16x16x16_bf16 v[206:209], v[20:21], v[200:201], v[206:209]
	v_mfma_f32_16x16x16_bf16 v[210:213], v[24:25], v[204:205], v[210:213]
	ds_read_b64_tr_b16 v[42:43], v248 offset:13824
	ds_read_b64_tr_b16 v[44:45], v248 offset:13856
	ds_read_b64_tr_b16 v[46:47], v248 offset:13888
	ds_read_b64_tr_b16 v[48:49], v248 offset:13920
	s_waitcnt lgkmcnt(11)
	v_mfma_f32_16x16x16_bf16 v[210:213], v[68:69], v[66:67], v[210:213]
	s_waitcnt lgkmcnt(10)
	v_mfma_f32_16x16x16_bf16 v[214:217], v[26:27], v[198:199], 0
	s_waitcnt lgkmcnt(9)
	v_mfma_f32_16x16x16_bf16 v[218:221], v[30:31], v[202:203], 0
	v_mfma_f32_16x16x16_bf16 v[214:217], v[28:29], v[200:201], v[214:217]
	v_mfma_f32_16x16x16_bf16 v[218:221], v[32:33], v[204:205], v[218:221]
	ds_read_b32 v50, v251 offset:33792
	ds_read_b32 v51, v251 offset:34048
	v_add_u32_e32 v246, 0x900, v246
	ds_read2_b64 v[76:79], v246 offset1:4
	ds_read2_b64 v[80:83], v246 offset0:8 offset1:12
	v_add_f32_e32 v206, v206, v210
	v_add_f32_e32 v207, v207, v211
	v_add_f32_e32 v208, v208, v212
	v_add_f32_e32 v209, v209, v213
	v_cvt_pk_bf16_f32 v242, v206, v207
	v_cvt_pk_bf16_f32 v243, v208, v209
	ds_read_b64_tr_b16 v[84:85], v250 offset:20736
	v_add_u32_e32 v252, 0xf00, v252
	s_waitcnt lgkmcnt(13)
	ds_read2_b64 v[86:89], v252 offset1:80
	v_mfma_f32_16x16x16_bf16 v[238:241], v[74:75], v[242:243], 0
	v_mfma_f32_16x16x16_bf16 v[214:217], v[70:71], v[66:67], v[214:217]
	s_waitcnt lgkmcnt(12)
	v_mfma_f32_16x16x16_bf16 v[2:5], v[34:35], v[66:67], v[2:5]
	v_mfma_f32_16x16x16_bf16 v[6:9], v[36:37], v[66:67], v[6:9]
	s_waitcnt lgkmcnt(10)
	v_mfma_f32_16x16x16_bf16 v[10:13], v[38:39], v[66:67], v[10:13]
	v_mfma_f32_16x16x16_bf16 v[14:17], v[40:41], v[66:67], v[14:17]
	ds_read2_b64 v[90:93], v252 offset0:160 offset1:240
	v_add_u32_e32 v247, 0x900, v247
	ds_read2_b64 v[26:29], v247 offset1:4
	ds_read2_b64 v[30:33], v247 offset0:8 offset1:12
	v_cvt_pk_bf16_f32 v244, -v238, -v239
	v_cvt_pk_bf16_f32 v245, -v240, -v241
	ds_read_b64_tr_b16 v[34:35], v248 offset:11520
	s_waitcnt lgkmcnt(13)
	ds_read_b64_tr_b16 v[36:37], v248 offset:11552
	s_waitcnt lgkmcnt(13)
	ds_read_b64_tr_b16 v[38:39], v248 offset:11584
	s_waitcnt lgkmcnt(13)
	ds_read_b64_tr_b16 v[40:41], v248 offset:11616
	v_mfma_f32_16x16x16_bf16 v[218:221], v[72:73], v[244:245], v[218:221]
	v_mfma_f32_16x16x16_bf16 v[2:5], v[42:43], v[244:245], v[2:5]
	v_mfma_f32_16x16x16_bf16 v[6:9], v[44:45], v[244:245], v[6:9]
	s_waitcnt lgkmcnt(13)
	v_mfma_f32_16x16x16_bf16 v[10:13], v[46:47], v[244:245], v[10:13]
	v_mfma_f32_16x16x16_bf16 v[14:17], v[48:49], v[244:245], v[14:17]
	ds_read_b64_tr_b16 v[42:43], v248 offset:16128
	s_waitcnt lgkmcnt(13)
	ds_read_b64_tr_b16 v[44:45], v248 offset:16160
	s_waitcnt lgkmcnt(13)
	ds_read_b64_tr_b16 v[46:47], v248 offset:16192
	s_waitcnt lgkmcnt(13)
	ds_read_b64_tr_b16 v[48:49], v248 offset:16224
	v_add_f32_e32 v214, v214, v218
	v_add_f32_e32 v215, v215, v219
	v_add_f32_e32 v216, v216, v220
	v_add_f32_e32 v217, v217, v221
	s_waitcnt lgkmcnt(13)
	ds_write2st64_b32 v253, v214, v215 offset0:0 offset1:1
	s_waitcnt lgkmcnt(13)
	ds_write2st64_b32 v253, v216, v217 offset0:2 offset1:3
	v_mul_f32_dpp v2, v50, v2 row_newbcast:0 row_mask:0xf bank_mask:0xf
	v_mul_f32_dpp v3, v50, v3 row_newbcast:1 row_mask:0xf bank_mask:0xf
	v_mul_f32_dpp v4, v50, v4 row_newbcast:2 row_mask:0xf bank_mask:0xf
	v_mul_f32_dpp v5, v50, v5 row_newbcast:3 row_mask:0xf bank_mask:0xf
	v_mul_f32_dpp v6, v50, v6 row_newbcast:4 row_mask:0xf bank_mask:0xf
	v_mul_f32_dpp v7, v50, v7 row_newbcast:5 row_mask:0xf bank_mask:0xf
	v_mul_f32_dpp v8, v50, v8 row_newbcast:6 row_mask:0xf bank_mask:0xf
	v_mul_f32_dpp v9, v50, v9 row_newbcast:7 row_mask:0xf bank_mask:0xf
	v_mul_f32_dpp v10, v50, v10 row_newbcast:8 row_mask:0xf bank_mask:0xf
	v_mul_f32_dpp v11, v50, v11 row_newbcast:9 row_mask:0xf bank_mask:0xf
	v_mul_f32_dpp v12, v50, v12 row_newbcast:10 row_mask:0xf bank_mask:0xf
	v_mul_f32_dpp v13, v50, v13 row_newbcast:11 row_mask:0xf bank_mask:0xf
	v_mul_f32_dpp v14, v50, v14 row_newbcast:12 row_mask:0xf bank_mask:0xf
	v_mul_f32_dpp v15, v50, v15 row_newbcast:13 row_mask:0xf bank_mask:0xf
	v_mul_f32_dpp v16, v50, v16 row_newbcast:14 row_mask:0xf bank_mask:0xf
	v_mul_f32_dpp v17, v50, v17 row_newbcast:15 row_mask:0xf bank_mask:0xf
	v_cvt_pk_bf16_f32 v198, v2, v3
	v_cvt_pk_bf16_f32 v199, v4, v5
	v_cvt_pk_bf16_f32 v202, v10, v11
	v_cvt_pk_bf16_f32 v203, v12, v13
	v_cvt_pk_bf16_f32 v200, v6, v7
	v_cvt_pk_bf16_f32 v201, v8, v9
	v_cvt_pk_bf16_f32 v204, v14, v15
	v_cvt_pk_bf16_f32 v205, v16, v17
	v_add_u32_e32 v246, v115, v155
	v_bfe_u32 v248, v0, 4, 2
	v_mul_u32_u24_e32 v248, 0x240, v248
	v_bfe_u32 v249, v0, 2, 2
	v_mul_u32_u24_e32 v249, 0x90, v249
	v_and_b32_e32 v250, 3, v0
	v_add_u32_e32 v248, v248, v249
	v_lshl_add_u32 v248, v250, 3, v248
	v_bfe_u32 v249, v0, 6, 2
	v_add_u32_e32 v246, 0x10c00, v246
	v_add_u32_e32 v248, 0x10c00, v248
	v_and_b32_e32 v251, 12, v0
	v_lshl_add_u32 v251, v251, 4, v113
	v_lshl_add_u32 v251, v250, 2, v251
	v_add_u32_e32 v251, 0x10c00, v251
	v_lshl_add_u32 v250, v249, 5, v248
	v_add_u32_e32 v247, 0x1200, v246
	s_waitcnt lgkmcnt(13)
	ds_read2_b64 v[18:21], v246 offset1:4
	s_waitcnt lgkmcnt(13)
	ds_read2_b64 v[22:25], v246 offset0:8 offset1:12
	s_waitcnt lgkmcnt(13)
	ds_read_b64_tr_b16 v[66:67], v250 offset:18432
	v_mfma_f32_16x16x16_bf16 v[206:209], v[76:77], v[198:199], 0
	v_mfma_f32_16x16x16_bf16 v[210:213], v[80:81], v[202:203], 0
	v_mfma_f32_16x16x16_bf16 v[206:209], v[78:79], v[200:201], v[206:209]
	v_mfma_f32_16x16x16_bf16 v[210:213], v[82:83], v[204:205], v[210:213]
	v_mfma_f32_16x16x16_bf16 v[210:213], v[86:87], v[84:85], v[210:213]
	v_mfma_f32_16x16x16_bf16 v[214:217], v[26:27], v[198:199], 0
	s_waitcnt lgkmcnt(13)
	v_mfma_f32_16x16x16_bf16 v[218:221], v[30:31], v[202:203], 0
	v_mfma_f32_16x16x16_bf16 v[214:217], v[28:29], v[200:201], v[214:217]
	v_mfma_f32_16x16x16_bf16 v[218:221], v[32:33], v[204:205], v[218:221]
	s_nop 2
	v_add_f32_e32 v206, v206, v210
	v_add_f32_e32 v207, v207, v211
	v_add_f32_e32 v208, v208, v212
	v_add_f32_e32 v209, v209, v213
	v_cvt_pk_bf16_f32 v242, v206, v207
	v_cvt_pk_bf16_f32 v243, v208, v209
	s_nop 1
	v_mfma_f32_16x16x16_bf16 v[238:241], v[92:93], v[242:243], 0
	v_mfma_f32_16x16x16_bf16 v[214:217], v[88:89], v[84:85], v[214:217]
	s_waitcnt lgkmcnt(11)
	v_mfma_f32_16x16x16_bf16 v[2:5], v[34:35], v[84:85], v[2:5]
	v_mfma_f32_16x16x16_bf16 v[6:9], v[36:37], v[84:85], v[6:9]
	s_waitcnt lgkmcnt(9)
	v_mfma_f32_16x16x16_bf16 v[10:13], v[38:39], v[84:85], v[10:13]
	v_mfma_f32_16x16x16_bf16 v[14:17], v[40:41], v[84:85], v[14:17]
	s_nop 0
	v_cvt_pk_bf16_f32 v244, -v238, -v239
	v_cvt_pk_bf16_f32 v245, -v240, -v241
	s_nop 1
	v_mfma_f32_16x16x16_bf16 v[218:221], v[90:91], v[244:245], v[218:221]
	s_waitcnt lgkmcnt(7)
	v_mfma_f32_16x16x16_bf16 v[2:5], v[42:43], v[244:245], v[2:5]
	v_mfma_f32_16x16x16_bf16 v[6:9], v[44:45], v[244:245], v[6:9]
	s_waitcnt lgkmcnt(5)
	v_mfma_f32_16x16x16_bf16 v[10:13], v[46:47], v[244:245], v[10:13]
	v_mfma_f32_16x16x16_bf16 v[14:17], v[48:49], v[244:245], v[14:17]
	s_nop 1
	v_add_f32_e32 v214, v214, v218
	v_add_f32_e32 v215, v215, v219
	v_add_f32_e32 v216, v216, v220
	v_add_f32_e32 v217, v217, v221
	ds_write2st64_b32 v253, v214, v215 offset0:16 offset1:17
	ds_write2st64_b32 v253, v216, v217 offset0:18 offset1:19
	v_mul_f32_dpp v2, v51, v2 row_newbcast:0 row_mask:0xf bank_mask:0xf
	v_mul_f32_dpp v3, v51, v3 row_newbcast:1 row_mask:0xf bank_mask:0xf
	v_mul_f32_dpp v4, v51, v4 row_newbcast:2 row_mask:0xf bank_mask:0xf
	v_mul_f32_dpp v5, v51, v5 row_newbcast:3 row_mask:0xf bank_mask:0xf
	v_mul_f32_dpp v6, v51, v6 row_newbcast:4 row_mask:0xf bank_mask:0xf
	v_mul_f32_dpp v7, v51, v7 row_newbcast:5 row_mask:0xf bank_mask:0xf
	v_mul_f32_dpp v8, v51, v8 row_newbcast:6 row_mask:0xf bank_mask:0xf
	v_mul_f32_dpp v9, v51, v9 row_newbcast:7 row_mask:0xf bank_mask:0xf
	v_mul_f32_dpp v10, v51, v10 row_newbcast:8 row_mask:0xf bank_mask:0xf
	v_mul_f32_dpp v11, v51, v11 row_newbcast:9 row_mask:0xf bank_mask:0xf
	v_mul_f32_dpp v12, v51, v12 row_newbcast:10 row_mask:0xf bank_mask:0xf
	v_mul_f32_dpp v13, v51, v13 row_newbcast:11 row_mask:0xf bank_mask:0xf
	v_mul_f32_dpp v14, v51, v14 row_newbcast:12 row_mask:0xf bank_mask:0xf
	v_mul_f32_dpp v15, v51, v15 row_newbcast:13 row_mask:0xf bank_mask:0xf
	v_mul_f32_dpp v16, v51, v16 row_newbcast:14 row_mask:0xf bank_mask:0xf
	v_mul_f32_dpp v17, v51, v17 row_newbcast:15 row_mask:0xf bank_mask:0xf
	s_branch .Lscan_join2

.LBB0_1160:
.Lscan_join2:
	s_waitcnt lgkmcnt(0)
	s_barrier
	v_readlane_b32 s0, v255, 17
	v_readlane_b32 s1, v255, 18
	s_and_b64 vcc, exec, s[0:1]
	s_mov_b64 s[30:31], -1
	s_cbranch_vccnz .LBB0_1162
	v_readlane_b32 s0, v255, 13
	s_nop 1
	s_nop 0
	s_mul_i32 s1, s0, 0x1e00
	s_lshl_b32 s0, s0, 13
	v_add_u32_e32 v252, s1, v166
	v_add_u32_e32 v253, s0, v165
	ds_read2_b64 v[68:71], v252 offset1:80
	v_cvt_pk_bf16_f32 v198, v2, v3
	v_cvt_pk_bf16_f32 v199, v4, v5
	v_cvt_pk_bf16_f32 v202, v10, v11
	v_cvt_pk_bf16_f32 v203, v12, v13
	v_cvt_pk_bf16_f32 v200, v6, v7
	v_cvt_pk_bf16_f32 v201, v8, v9
	v_cvt_pk_bf16_f32 v204, v14, v15
	v_cvt_pk_bf16_f32 v205, v16, v17
	ds_read2_b64 v[26:29], v247 offset1:4
	ds_read2_b64 v[30:33], v247 offset0:8 offset1:12
	ds_read2_b64 v[72:75], v252 offset0:160 offset1:240
	v_mfma_f32_16x16x16_bf16 v[206:209], v[18:19], v[198:199], 0
	v_mfma_f32_16x16x16_bf16 v[210:213], v[22:23], v[202:203], 0
	ds_read_b64_tr_b16 v[34:35], v248 offset:9216
	ds_read_b64_tr_b16 v[36:37], v248 offset:9248
	ds_read_b64_tr_b16 v[38:39], v248 offset:9280
	ds_read_b64_tr_b16 v[40:41], v248 offset:9312
	v_mfma_f32_16x16x16_bf16 v[206:209], v[20:21], v[200:201], v[206:209]
	v_mfma_f32_16x16x16_bf16 v[210:213], v[24:25], v[204:205], v[210:213]
	ds_read_b64_tr_b16 v[42:43], v248 offset:13824
	ds_read_b64_tr_b16 v[44:45], v248 offset:13856
	ds_read_b64_tr_b16 v[46:47], v248 offset:13888
	ds_read_b64_tr_b16 v[48:49], v248 offset:13920
	s_waitcnt lgkmcnt(11)
	v_mfma_f32_16x16x16_bf16 v[210:213], v[68:69], v[66:67], v[210:213]
	s_waitcnt lgkmcnt(10)
	v_mfma_f32_16x16x16_bf16 v[214:217], v[26:27], v[198:199], 0
	s_waitcnt lgkmcnt(9)
	v_mfma_f32_16x16x16_bf16 v[218:221], v[30:31], v[202:203], 0
	v_mfma_f32_16x16x16_bf16 v[214:217], v[28:29], v[200:201], v[214:217]
	v_mfma_f32_16x16x16_bf16 v[218:221], v[32:33], v[204:205], v[218:221]
	ds_read_b32 v50, v251 offset:33792
	ds_read_b32 v51, v251 offset:34048
	v_add_u32_e32 v246, 0x900, v246
	ds_read2_b64 v[76:79], v246 offset1:4
	ds_read2_b64 v[80:83], v246 offset0:8 offset1:12
	v_add_f32_e32 v206, v206, v210
	v_add_f32_e32 v207, v207, v211
	v_add_f32_e32 v208, v208, v212
	v_add_f32_e32 v209, v209, v213
	v_cvt_pk_bf16_f32 v242, v206, v207
	v_cvt_pk_bf16_f32 v243, v208, v209
	ds_read_b64_tr_b16 v[84:85], v250 offset:20736
	v_add_u32_e32 v252, 0xf00, v252
	s_waitcnt lgkmcnt(13)
	ds_read2_b64 v[86:89], v252 offset1:80
	v_mfma_f32_16x16x16_bf16 v[238:241], v[74:75], v[242:243], 0
	v_mfma_f32_16x16x16_bf16 v[214:217], v[70:71], v[66:67], v[214:217]
	s_waitcnt lgkmcnt(12)
	v_mfma_f32_16x16x16_bf16 v[2:5], v[34:35], v[66:67], v[2:5]
	v_mfma_f32_16x16x16_bf16 v[6:9], v[36:37], v[66:67], v[6:9]
	s_waitcnt lgkmcnt(10)
	v_mfma_f32_16x16x16_bf16 v[10:13], v[38:39], v[66:67], v[10:13]
	v_mfma_f32_16x16x16_bf16 v[14:17], v[40:41], v[66:67], v[14:17]
	ds_read2_b64 v[90:93], v252 offset0:160 offset1:240
	v_add_u32_e32 v247, 0x900, v247
	ds_read2_b64 v[26:29], v247 offset1:4
	ds_read2_b64 v[30:33], v247 offset0:8 offset1:12
	v_cvt_pk_bf16_f32 v244, -v238, -v239
	v_cvt_pk_bf16_f32 v245, -v240, -v241
	ds_read_b64_tr_b16 v[34:35], v248 offset:11520
	s_waitcnt lgkmcnt(13)
	ds_read_b64_tr_b16 v[36:37], v248 offset:11552
	s_waitcnt lgkmcnt(13)
	ds_read_b64_tr_b16 v[38:39], v248 offset:11584
	s_waitcnt lgkmcnt(13)
	ds_read_b64_tr_b16 v[40:41], v248 offset:11616
	v_mfma_f32_16x16x16_bf16 v[218:221], v[72:73], v[244:245], v[218:221]
	v_mfma_f32_16x16x16_bf16 v[2:5], v[42:43], v[244:245], v[2:5]
	v_mfma_f32_16x16x16_bf16 v[6:9], v[44:45], v[244:245], v[6:9]
	s_waitcnt lgkmcnt(13)
	v_mfma_f32_16x16x16_bf16 v[10:13], v[46:47], v[244:245], v[10:13]
	v_mfma_f32_16x16x16_bf16 v[14:17], v[48:49], v[244:245], v[14:17]
	ds_read_b64_tr_b16 v[42:43], v248 offset:16128
	s_waitcnt lgkmcnt(13)
	ds_read_b64_tr_b16 v[44:45], v248 offset:16160
	s_waitcnt lgkmcnt(13)
	ds_read_b64_tr_b16 v[46:47], v248 offset:16192
	s_waitcnt lgkmcnt(13)
	ds_read_b64_tr_b16 v[48:49], v248 offset:16224
	v_add_f32_e32 v214, v214, v218
	v_add_f32_e32 v215, v215, v219
	v_add_f32_e32 v216, v216, v220
	v_add_f32_e32 v217, v217, v221
	s_waitcnt lgkmcnt(13)
	ds_write2st64_b32 v253, v214, v215 offset0:0 offset1:1
	s_waitcnt lgkmcnt(13)
	ds_write2st64_b32 v253, v216, v217 offset0:2 offset1:3
	v_mul_f32_dpp v2, v50, v2 row_newbcast:0 row_mask:0xf bank_mask:0xf
	v_mul_f32_dpp v3, v50, v3 row_newbcast:1 row_mask:0xf bank_mask:0xf
	v_mul_f32_dpp v4, v50, v4 row_newbcast:2 row_mask:0xf bank_mask:0xf
	v_mul_f32_dpp v5, v50, v5 row_newbcast:3 row_mask:0xf bank_mask:0xf
	v_mul_f32_dpp v6, v50, v6 row_newbcast:4 row_mask:0xf bank_mask:0xf
	v_mul_f32_dpp v7, v50, v7 row_newbcast:5 row_mask:0xf bank_mask:0xf
	v_mul_f32_dpp v8, v50, v8 row_newbcast:6 row_mask:0xf bank_mask:0xf
	v_mul_f32_dpp v9, v50, v9 row_newbcast:7 row_mask:0xf bank_mask:0xf
	v_mul_f32_dpp v10, v50, v10 row_newbcast:8 row_mask:0xf bank_mask:0xf
	v_mul_f32_dpp v11, v50, v11 row_newbcast:9 row_mask:0xf bank_mask:0xf
	v_mul_f32_dpp v12, v50, v12 row_newbcast:10 row_mask:0xf bank_mask:0xf
	v_mul_f32_dpp v13, v50, v13 row_newbcast:11 row_mask:0xf bank_mask:0xf
	v_mul_f32_dpp v14, v50, v14 row_newbcast:12 row_mask:0xf bank_mask:0xf
	v_mul_f32_dpp v15, v50, v15 row_newbcast:13 row_mask:0xf bank_mask:0xf
	v_mul_f32_dpp v16, v50, v16 row_newbcast:14 row_mask:0xf bank_mask:0xf
	v_mul_f32_dpp v17, v50, v17 row_newbcast:15 row_mask:0xf bank_mask:0xf
	v_cvt_pk_bf16_f32 v198, v2, v3
	v_cvt_pk_bf16_f32 v199, v4, v5
	v_cvt_pk_bf16_f32 v202, v10, v11
	v_cvt_pk_bf16_f32 v203, v12, v13
	v_cvt_pk_bf16_f32 v200, v6, v7
	v_cvt_pk_bf16_f32 v201, v8, v9
	v_cvt_pk_bf16_f32 v204, v14, v15
	v_cvt_pk_bf16_f32 v205, v16, v17
	v_add_u32_e32 v246, v115, v155
	v_bfe_u32 v248, v0, 4, 2
	v_mul_u32_u24_e32 v248, 0x240, v248
	v_bfe_u32 v249, v0, 2, 2
	v_mul_u32_u24_e32 v249, 0x90, v249
	v_and_b32_e32 v250, 3, v0
	v_add_u32_e32 v248, v248, v249
	v_lshl_add_u32 v248, v250, 3, v248
	v_bfe_u32 v249, v0, 6, 2
	v_and_b32_e32 v251, 12, v0
	v_lshl_add_u32 v251, v251, 4, v113
	v_lshl_add_u32 v251, v250, 2, v251
	v_lshl_add_u32 v250, v249, 5, v248
	v_add_u32_e32 v247, 0x1200, v246
	s_waitcnt lgkmcnt(13)
	ds_read2_b64 v[18:21], v246 offset1:4
	s_waitcnt lgkmcnt(13)
	ds_read2_b64 v[22:25], v246 offset0:8 offset1:12
	s_waitcnt lgkmcnt(13)
	ds_read_b64_tr_b16 v[66:67], v250 offset:18432
	v_mfma_f32_16x16x16_bf16 v[206:209], v[76:77], v[198:199], 0
	v_mfma_f32_16x16x16_bf16 v[210:213], v[80:81], v[202:203], 0
	v_mfma_f32_16x16x16_bf16 v[206:209], v[78:79], v[200:201], v[206:209]
	v_mfma_f32_16x16x16_bf16 v[210:213], v[82:83], v[204:205], v[210:213]
	v_mfma_f32_16x16x16_bf16 v[210:213], v[86:87], v[84:85], v[210:213]
	v_mfma_f32_16x16x16_bf16 v[214:217], v[26:27], v[198:199], 0
	s_waitcnt lgkmcnt(13)
	v_mfma_f32_16x16x16_bf16 v[218:221], v[30:31], v[202:203], 0
	v_mfma_f32_16x16x16_bf16 v[214:217], v[28:29], v[200:201], v[214:217]
	v_mfma_f32_16x16x16_bf16 v[218:221], v[32:33], v[204:205], v[218:221]
	s_nop 2
	v_add_f32_e32 v206, v206, v210
	v_add_f32_e32 v207, v207, v211
	v_add_f32_e32 v208, v208, v212
	v_add_f32_e32 v209, v209, v213
	v_cvt_pk_bf16_f32 v242, v206, v207
	v_cvt_pk_bf16_f32 v243, v208, v209
	s_nop 1
	v_mfma_f32_16x16x16_bf16 v[238:241], v[92:93], v[242:243], 0
	v_mfma_f32_16x16x16_bf16 v[214:217], v[88:89], v[84:85], v[214:217]
	s_waitcnt lgkmcnt(11)
	v_mfma_f32_16x16x16_bf16 v[2:5], v[34:35], v[84:85], v[2:5]
	v_mfma_f32_16x16x16_bf16 v[6:9], v[36:37], v[84:85], v[6:9]
	s_waitcnt lgkmcnt(9)
	v_mfma_f32_16x16x16_bf16 v[10:13], v[38:39], v[84:85], v[10:13]
	v_mfma_f32_16x16x16_bf16 v[14:17], v[40:41], v[84:85], v[14:17]
	s_nop 0
	v_cvt_pk_bf16_f32 v244, -v238, -v239
	v_cvt_pk_bf16_f32 v245, -v240, -v241
	s_nop 1
	v_mfma_f32_16x16x16_bf16 v[218:221], v[90:91], v[244:245], v[218:221]
	s_waitcnt lgkmcnt(7)
	v_mfma_f32_16x16x16_bf16 v[2:5], v[42:43], v[244:245], v[2:5]
	v_mfma_f32_16x16x16_bf16 v[6:9], v[44:45], v[244:245], v[6:9]
	s_waitcnt lgkmcnt(5)
	v_mfma_f32_16x16x16_bf16 v[10:13], v[46:47], v[244:245], v[10:13]
	v_mfma_f32_16x16x16_bf16 v[14:17], v[48:49], v[244:245], v[14:17]
	s_nop 1
	v_add_f32_e32 v214, v214, v218
	v_add_f32_e32 v215, v215, v219
	v_add_f32_e32 v216, v216, v220
	v_add_f32_e32 v217, v217, v221
	ds_write2st64_b32 v253, v214, v215 offset0:16 offset1:17
	ds_write2st64_b32 v253, v216, v217 offset0:18 offset1:19
	v_mul_f32_dpp v2, v51, v2 row_newbcast:0 row_mask:0xf bank_mask:0xf
	v_mul_f32_dpp v3, v51, v3 row_newbcast:1 row_mask:0xf bank_mask:0xf
	v_mul_f32_dpp v4, v51, v4 row_newbcast:2 row_mask:0xf bank_mask:0xf
	v_mul_f32_dpp v5, v51, v5 row_newbcast:3 row_mask:0xf bank_mask:0xf
	v_mul_f32_dpp v6, v51, v6 row_newbcast:4 row_mask:0xf bank_mask:0xf
	v_mul_f32_dpp v7, v51, v7 row_newbcast:5 row_mask:0xf bank_mask:0xf
	v_mul_f32_dpp v8, v51, v8 row_newbcast:6 row_mask:0xf bank_mask:0xf
	v_mul_f32_dpp v9, v51, v9 row_newbcast:7 row_mask:0xf bank_mask:0xf
	v_mul_f32_dpp v10, v51, v10 row_newbcast:8 row_mask:0xf bank_mask:0xf
	v_mul_f32_dpp v11, v51, v11 row_newbcast:9 row_mask:0xf bank_mask:0xf
	v_mul_f32_dpp v12, v51, v12 row_newbcast:10 row_mask:0xf bank_mask:0xf
	v_mul_f32_dpp v13, v51, v13 row_newbcast:11 row_mask:0xf bank_mask:0xf
	v_mul_f32_dpp v14, v51, v14 row_newbcast:12 row_mask:0xf bank_mask:0xf
	v_mul_f32_dpp v15, v51, v15 row_newbcast:13 row_mask:0xf bank_mask:0xf
	v_mul_f32_dpp v16, v51, v16 row_newbcast:14 row_mask:0xf bank_mask:0xf
	v_mul_f32_dpp v17, v51, v17 row_newbcast:15 row_mask:0xf bank_mask:0xf
	s_branch .Lscan_join3
